# K1: next iteration's loads issued in two halves, each right after its rows' raw data is consumed (finer-grained software pipeline)
# speedup vs baseline: 1.0017x; 1.0017x over previous
.LBB0_8:
	s_bitcmp1_b32 s15, 8
	s_cselect_b64 s[20:21], -1, 0
	s_lshr_b32 s16, s15, 2
	s_and_b32 s16, s16, 63
	s_lshl_b64 s[4:5], 1, s16
	s_waitcnt vmcnt(12)
	v_pk_add_f32 v[72:73], v[26:27], v[28:29]
	v_pk_add_f32 v[74:75], v[10:11], v[12:13]
	v_pk_add_f32 v[76:77], v[34:35], v[36:37]
	v_pk_add_f32 v[78:79], v[14:15], v[16:17]
	v_pk_add_f32 v[58:59], v[26:27], v[34:35]
	v_pk_add_f32 v[60:61], v[28:29], v[36:37]
	v_pk_add_f32 v[72:73], v[72:73], v[74:75]
	v_pk_add_f32 v[76:77], v[76:77], v[78:79]
	v_pk_add_f32 v[54:55], v[10:11], v[14:15]
	v_pk_add_f32 v[56:57], v[12:13], v[16:17]
	v_add_f32_e32 v50, v72, v73
	v_add_f32_e32 v51, v76, v77
	v_cndmask_b32_e64 v64, v26, v10, s[20:21]
	v_cndmask_b32_e64 v65, v35, v15, s[20:21]
	v_add_u32_e32 v46, 0x10000, v68
	buffer_load_dwordx4 v[26:29], v46, s[8:11], 0 offen sc0 nt
	buffer_load_dwordx4 v[10:13], v46, s[8:11], 0 offen offset:1024 sc0 nt
	buffer_load_dwordx4 v[34:37], v46, s[8:11], 0 offen offset:2048 sc0 nt
	buffer_load_dwordx4 v[14:17], v46, s[8:11], 0 offen offset:3072 sc0 nt
	s_waitcnt vmcnt(12)
	v_pk_add_f32 v[72:73], v[30:31], v[32:33]
	v_pk_add_f32 v[74:75], v[18:19], v[20:21]
	v_pk_add_f32 v[76:77], v[38:39], v[40:41]
	v_pk_add_f32 v[78:79], v[22:23], v[24:25]
	v_pk_add_f32 v[48:49], v[30:31], v[38:39]
	v_pk_add_f32 v[70:71], v[32:33], v[40:41]
	v_pk_add_f32 v[72:73], v[72:73], v[74:75]
	v_pk_add_f32 v[76:77], v[76:77], v[78:79]
	v_pk_add_f32 v[58:59], v[58:59], v[48:49]
	v_pk_add_f32 v[60:61], v[60:61], v[70:71]
	v_pk_add_f32 v[48:49], v[18:19], v[22:23]
	v_pk_add_f32 v[70:71], v[20:21], v[24:25]
	v_add_f32_e32 v52, v72, v73
	v_add_f32_e32 v53, v76, v77
	v_cndmask_b32_e64 v66, v32, v20, s[20:21]
	v_cndmask_b32_e64 v67, v41, v25, s[20:21]
	v_add_u32_e32 v46, 0x11000, v68
	buffer_load_dwordx4 v[30:33], v46, s[8:11], 0 offen sc0 nt
	buffer_load_dwordx4 v[18:21], v46, s[8:11], 0 offen offset:1024 sc0 nt
	buffer_load_dwordx4 v[38:41], v46, s[8:11], 0 offen offset:2048 sc0 nt
	buffer_load_dwordx4 v[22:25], v46, s[8:11], 0 offen offset:3072 sc0 nt
	v_pk_add_f32 v[2:3], v[2:3], v[58:59]
	v_pk_add_f32 v[4:5], v[4:5], v[60:61]
	v_pk_add_f32 v[54:55], v[54:55], v[48:49]
	v_pk_add_f32 v[56:57], v[56:57], v[70:71]
	v_pk_add_f32 v[6:7], v[6:7], v[54:55]
	v_pk_add_f32 v[8:9], v[8:9], v[56:57]
	v_add_f32_dpp v50, v50, v50 quad_perm:[1,0,3,2] row_mask:0xf bank_mask:0xf
	v_add_f32_dpp v51, v51, v51 quad_perm:[1,0,3,2] row_mask:0xf bank_mask:0xf
	v_add_f32_dpp v52, v52, v52 quad_perm:[1,0,3,2] row_mask:0xf bank_mask:0xf
	v_add_f32_dpp v53, v53, v53 quad_perm:[1,0,3,2] row_mask:0xf bank_mask:0xf
	v_add_f32_dpp v50, v50, v50 quad_perm:[2,3,0,1] row_mask:0xf bank_mask:0xf
	v_add_f32_dpp v51, v51, v51 quad_perm:[2,3,0,1] row_mask:0xf bank_mask:0xf
	v_add_f32_dpp v52, v52, v52 quad_perm:[2,3,0,1] row_mask:0xf bank_mask:0xf
	v_add_f32_dpp v53, v53, v53 quad_perm:[2,3,0,1] row_mask:0xf bank_mask:0xf
	v_add_f32_dpp v50, v50, v50 row_half_mirror row_mask:0xf bank_mask:0xf
	v_add_f32_dpp v51, v51, v51 row_half_mirror row_mask:0xf bank_mask:0xf
	v_add_f32_dpp v52, v52, v52 row_half_mirror row_mask:0xf bank_mask:0xf
	v_add_f32_dpp v53, v53, v53 row_half_mirror row_mask:0xf bank_mask:0xf
	v_add_f32_dpp v50, v50, v50 row_mirror row_mask:0xf bank_mask:0xf
	v_add_f32_dpp v51, v51, v51 row_mirror row_mask:0xf bank_mask:0xf
	v_add_f32_dpp v52, v52, v52 row_mirror row_mask:0xf bank_mask:0xf
	v_add_f32_dpp v53, v53, v53 row_mirror row_mask:0xf bank_mask:0xf
	v_add_f32_dpp v50, v50, v50 row_bcast:15 row_mask:0xa bank_mask:0xf
	v_add_f32_dpp v51, v51, v51 row_bcast:15 row_mask:0xa bank_mask:0xf
	v_add_f32_dpp v52, v52, v52 row_bcast:15 row_mask:0xa bank_mask:0xf
	v_add_f32_dpp v53, v53, v53 row_bcast:15 row_mask:0xa bank_mask:0xf
	v_add_f32_dpp v50, v50, v50 row_bcast:31 row_mask:0xc bank_mask:0xf
	v_add_f32_dpp v51, v51, v51 row_bcast:31 row_mask:0xc bank_mask:0xf
	v_add_f32_dpp v52, v52, v52 row_bcast:31 row_mask:0xc bank_mask:0xf
	v_add_f32_dpp v53, v53, v53 row_bcast:31 row_mask:0xc bank_mask:0xf
	s_mov_b64 exec, s[4:5]
	global_store_dwordx4 v[44:45], v[64:67], off
	v_add_f32_e32 v72, v64, v65
	v_add_f32_e32 v73, v66, v67
	v_add_f32_e32 v72, v72, v73
	v_add_f32_e32 v42, v42, v72
	s_mov_b32 s4, 0
	s_brev_b32 s5, 1
	s_mov_b64 exec, s[4:5]
	v_lshl_add_u64 v[72:73], v[44:45], 0, s[18:19]
	global_store_dwordx4 v[72:73], v[50:53], off
	s_mov_b64 exec, -1
	s_add_u32 s15, s15, 16
	v_lshl_add_u64 v[44:45], v[44:45], 0, 64
	s_bitcmp1_b32 s15, 8
	s_cselect_b64 s[20:21], -1, 0
	s_lshr_b32 s16, s15, 2
	s_and_b32 s16, s16, 63
	s_lshl_b64 s[4:5], 1, s16
	s_waitcnt vmcnt(14)
	v_pk_add_f32 v[72:73], v[96:97], v[98:99]
	v_pk_add_f32 v[74:75], v[80:81], v[82:83]
	v_pk_add_f32 v[76:77], v[104:105], v[106:107]
	v_pk_add_f32 v[78:79], v[84:85], v[86:87]
	v_pk_add_f32 v[58:59], v[96:97], v[104:105]
	v_pk_add_f32 v[60:61], v[98:99], v[106:107]
	v_pk_add_f32 v[72:73], v[72:73], v[74:75]
	v_pk_add_f32 v[76:77], v[76:77], v[78:79]
	v_pk_add_f32 v[54:55], v[80:81], v[84:85]
	v_pk_add_f32 v[56:57], v[82:83], v[86:87]
	v_add_f32_e32 v50, v72, v73
	v_add_f32_e32 v51, v76, v77
	v_cndmask_b32_e64 v64, v96, v80, s[20:21]
	v_cndmask_b32_e64 v65, v105, v85, s[20:21]
	v_add_u32_e32 v46, 0x18000, v68
	buffer_load_dwordx4 v[96:99], v46, s[8:11], 0 offen sc0 nt
	buffer_load_dwordx4 v[80:83], v46, s[8:11], 0 offen offset:1024 sc0 nt
	buffer_load_dwordx4 v[104:107], v46, s[8:11], 0 offen offset:2048 sc0 nt
	buffer_load_dwordx4 v[84:87], v46, s[8:11], 0 offen offset:3072 sc0 nt
	s_waitcnt vmcnt(14)
	v_pk_add_f32 v[72:73], v[100:101], v[102:103]
	v_pk_add_f32 v[74:75], v[88:89], v[90:91]
	v_pk_add_f32 v[76:77], v[108:109], v[110:111]
	v_pk_add_f32 v[78:79], v[92:93], v[94:95]
	v_pk_add_f32 v[48:49], v[100:101], v[108:109]
	v_pk_add_f32 v[70:71], v[102:103], v[110:111]
	v_pk_add_f32 v[72:73], v[72:73], v[74:75]
	v_pk_add_f32 v[76:77], v[76:77], v[78:79]
	v_pk_add_f32 v[58:59], v[58:59], v[48:49]
	v_pk_add_f32 v[60:61], v[60:61], v[70:71]
	v_pk_add_f32 v[48:49], v[88:89], v[92:93]
	v_pk_add_f32 v[70:71], v[90:91], v[94:95]
	v_add_f32_e32 v52, v72, v73
	v_add_f32_e32 v53, v76, v77
	v_cndmask_b32_e64 v66, v102, v90, s[20:21]
	v_cndmask_b32_e64 v67, v111, v95, s[20:21]
	v_add_u32_e32 v46, 0x19000, v68
	buffer_load_dwordx4 v[100:103], v46, s[8:11], 0 offen sc0 nt
	buffer_load_dwordx4 v[88:91], v46, s[8:11], 0 offen offset:1024 sc0 nt
	buffer_load_dwordx4 v[108:111], v46, s[8:11], 0 offen offset:2048 sc0 nt
	buffer_load_dwordx4 v[92:95], v46, s[8:11], 0 offen offset:3072 sc0 nt
	v_pk_add_f32 v[2:3], v[2:3], v[58:59]
	v_pk_add_f32 v[4:5], v[4:5], v[60:61]
	v_pk_add_f32 v[54:55], v[54:55], v[48:49]
	v_pk_add_f32 v[56:57], v[56:57], v[70:71]
	v_pk_add_f32 v[6:7], v[6:7], v[54:55]
	v_pk_add_f32 v[8:9], v[8:9], v[56:57]
	v_add_f32_dpp v50, v50, v50 quad_perm:[1,0,3,2] row_mask:0xf bank_mask:0xf
	v_add_f32_dpp v51, v51, v51 quad_perm:[1,0,3,2] row_mask:0xf bank_mask:0xf
	v_add_f32_dpp v52, v52, v52 quad_perm:[1,0,3,2] row_mask:0xf bank_mask:0xf
	v_add_f32_dpp v53, v53, v53 quad_perm:[1,0,3,2] row_mask:0xf bank_mask:0xf
	v_add_f32_dpp v50, v50, v50 quad_perm:[2,3,0,1] row_mask:0xf bank_mask:0xf
	v_add_f32_dpp v51, v51, v51 quad_perm:[2,3,0,1] row_mask:0xf bank_mask:0xf
	v_add_f32_dpp v52, v52, v52 quad_perm:[2,3,0,1] row_mask:0xf bank_mask:0xf
	v_add_f32_dpp v53, v53, v53 quad_perm:[2,3,0,1] row_mask:0xf bank_mask:0xf
	v_add_f32_dpp v50, v50, v50 row_half_mirror row_mask:0xf bank_mask:0xf
	v_add_f32_dpp v51, v51, v51 row_half_mirror row_mask:0xf bank_mask:0xf
	v_add_f32_dpp v52, v52, v52 row_half_mirror row_mask:0xf bank_mask:0xf
	v_add_f32_dpp v53, v53, v53 row_half_mirror row_mask:0xf bank_mask:0xf
	v_add_f32_dpp v50, v50, v50 row_mirror row_mask:0xf bank_mask:0xf
	v_add_f32_dpp v51, v51, v51 row_mirror row_mask:0xf bank_mask:0xf
	v_add_f32_dpp v52, v52, v52 row_mirror row_mask:0xf bank_mask:0xf
	v_add_f32_dpp v53, v53, v53 row_mirror row_mask:0xf bank_mask:0xf
	v_add_f32_dpp v50, v50, v50 row_bcast:15 row_mask:0xa bank_mask:0xf
	v_add_f32_dpp v51, v51, v51 row_bcast:15 row_mask:0xa bank_mask:0xf
	v_add_f32_dpp v52, v52, v52 row_bcast:15 row_mask:0xa bank_mask:0xf
	v_add_f32_dpp v53, v53, v53 row_bcast:15 row_mask:0xa bank_mask:0xf
	v_add_f32_dpp v50, v50, v50 row_bcast:31 row_mask:0xc bank_mask:0xf
	v_add_f32_dpp v51, v51, v51 row_bcast:31 row_mask:0xc bank_mask:0xf
	v_add_f32_dpp v52, v52, v52 row_bcast:31 row_mask:0xc bank_mask:0xf
	v_add_f32_dpp v53, v53, v53 row_bcast:31 row_mask:0xc bank_mask:0xf
	s_mov_b64 exec, s[4:5]
	global_store_dwordx4 v[44:45], v[64:67], off
	v_add_f32_e32 v72, v64, v65
	v_add_f32_e32 v73, v66, v67
	v_add_f32_e32 v72, v72, v73
	v_add_f32_e32 v42, v42, v72
	s_mov_b32 s4, 0
	s_brev_b32 s5, 1
	s_mov_b64 exec, s[4:5]
	v_lshl_add_u64 v[72:73], v[44:45], 0, s[18:19]
	global_store_dwordx4 v[72:73], v[50:53], off
	s_mov_b64 exec, -1
	s_add_u32 s15, s15, 16
	v_lshl_add_u64 v[44:45], v[44:45], 0, 64
	s_bitcmp1_b32 s15, 8
	s_cselect_b64 s[20:21], -1, 0
	s_lshr_b32 s16, s15, 2
	s_and_b32 s16, s16, 63
	s_lshl_b64 s[4:5], 1, s16
	s_waitcnt vmcnt(16)
	v_pk_add_f32 v[72:73], v[26:27], v[28:29]
	v_pk_add_f32 v[74:75], v[10:11], v[12:13]
	v_pk_add_f32 v[76:77], v[34:35], v[36:37]
	v_pk_add_f32 v[78:79], v[14:15], v[16:17]
	v_pk_add_f32 v[58:59], v[26:27], v[34:35]
	v_pk_add_f32 v[60:61], v[28:29], v[36:37]
	v_pk_add_f32 v[72:73], v[72:73], v[74:75]
	v_pk_add_f32 v[76:77], v[76:77], v[78:79]
	v_pk_add_f32 v[54:55], v[10:11], v[14:15]
	v_pk_add_f32 v[56:57], v[12:13], v[16:17]
	v_add_f32_e32 v50, v72, v73
	v_add_f32_e32 v51, v76, v77
	v_cndmask_b32_e64 v64, v26, v10, s[20:21]
	v_cndmask_b32_e64 v65, v35, v15, s[20:21]
	s_waitcnt vmcnt(12)
	v_pk_add_f32 v[72:73], v[30:31], v[32:33]
	v_pk_add_f32 v[74:75], v[18:19], v[20:21]
	v_pk_add_f32 v[76:77], v[38:39], v[40:41]
	v_pk_add_f32 v[78:79], v[22:23], v[24:25]
	v_pk_add_f32 v[48:49], v[30:31], v[38:39]
	v_pk_add_f32 v[70:71], v[32:33], v[40:41]
	v_pk_add_f32 v[72:73], v[72:73], v[74:75]
	v_pk_add_f32 v[76:77], v[76:77], v[78:79]
	v_pk_add_f32 v[58:59], v[58:59], v[48:49]
	v_pk_add_f32 v[60:61], v[60:61], v[70:71]
	v_pk_add_f32 v[48:49], v[18:19], v[22:23]
	v_pk_add_f32 v[70:71], v[20:21], v[24:25]
	v_add_f32_e32 v52, v72, v73
	v_add_f32_e32 v53, v76, v77
	v_cndmask_b32_e64 v66, v32, v20, s[20:21]
	v_cndmask_b32_e64 v67, v41, v25, s[20:21]
	v_pk_add_f32 v[2:3], v[2:3], v[58:59]
	v_pk_add_f32 v[4:5], v[4:5], v[60:61]
	v_pk_add_f32 v[54:55], v[54:55], v[48:49]
	v_pk_add_f32 v[56:57], v[56:57], v[70:71]
	v_pk_add_f32 v[6:7], v[6:7], v[54:55]
	v_pk_add_f32 v[8:9], v[8:9], v[56:57]
	v_add_f32_dpp v50, v50, v50 quad_perm:[1,0,3,2] row_mask:0xf bank_mask:0xf
	v_add_f32_dpp v51, v51, v51 quad_perm:[1,0,3,2] row_mask:0xf bank_mask:0xf
	v_add_f32_dpp v52, v52, v52 quad_perm:[1,0,3,2] row_mask:0xf bank_mask:0xf
	v_add_f32_dpp v53, v53, v53 quad_perm:[1,0,3,2] row_mask:0xf bank_mask:0xf
	v_add_f32_dpp v50, v50, v50 quad_perm:[2,3,0,1] row_mask:0xf bank_mask:0xf
	v_add_f32_dpp v51, v51, v51 quad_perm:[2,3,0,1] row_mask:0xf bank_mask:0xf
	v_add_f32_dpp v52, v52, v52 quad_perm:[2,3,0,1] row_mask:0xf bank_mask:0xf
	v_add_f32_dpp v53, v53, v53 quad_perm:[2,3,0,1] row_mask:0xf bank_mask:0xf
	v_add_f32_dpp v50, v50, v50 row_half_mirror row_mask:0xf bank_mask:0xf
	v_add_f32_dpp v51, v51, v51 row_half_mirror row_mask:0xf bank_mask:0xf
	v_add_f32_dpp v52, v52, v52 row_half_mirror row_mask:0xf bank_mask:0xf
	v_add_f32_dpp v53, v53, v53 row_half_mirror row_mask:0xf bank_mask:0xf
	v_add_f32_dpp v50, v50, v50 row_mirror row_mask:0xf bank_mask:0xf
	v_add_f32_dpp v51, v51, v51 row_mirror row_mask:0xf bank_mask:0xf
	v_add_f32_dpp v52, v52, v52 row_mirror row_mask:0xf bank_mask:0xf
	v_add_f32_dpp v53, v53, v53 row_mirror row_mask:0xf bank_mask:0xf
	v_add_f32_dpp v50, v50, v50 row_bcast:15 row_mask:0xa bank_mask:0xf
	v_add_f32_dpp v51, v51, v51 row_bcast:15 row_mask:0xa bank_mask:0xf
	v_add_f32_dpp v52, v52, v52 row_bcast:15 row_mask:0xa bank_mask:0xf
	v_add_f32_dpp v53, v53, v53 row_bcast:15 row_mask:0xa bank_mask:0xf
	v_add_f32_dpp v50, v50, v50 row_bcast:31 row_mask:0xc bank_mask:0xf
	v_add_f32_dpp v51, v51, v51 row_bcast:31 row_mask:0xc bank_mask:0xf
	v_add_f32_dpp v52, v52, v52 row_bcast:31 row_mask:0xc bank_mask:0xf
	v_add_f32_dpp v53, v53, v53 row_bcast:31 row_mask:0xc bank_mask:0xf
	s_mov_b64 exec, s[4:5]
	global_store_dwordx4 v[44:45], v[64:67], off
	v_add_f32_e32 v72, v64, v65
	v_add_f32_e32 v73, v66, v67
	v_add_f32_e32 v72, v72, v73
	v_add_f32_e32 v42, v42, v72
	s_mov_b32 s4, 0
	s_brev_b32 s5, 1
	s_mov_b64 exec, s[4:5]
	v_lshl_add_u64 v[72:73], v[44:45], 0, s[18:19]
	global_store_dwordx4 v[72:73], v[50:53], off
	s_mov_b64 exec, -1
	s_add_u32 s15, s15, 16
	v_lshl_add_u64 v[44:45], v[44:45], 0, 64
	s_bitcmp1_b32 s15, 8
	s_cselect_b64 s[20:21], -1, 0
	s_lshr_b32 s16, s15, 2
	s_and_b32 s16, s16, 63
	s_lshl_b64 s[4:5], 1, s16
	s_waitcnt vmcnt(8)
	v_pk_add_f32 v[72:73], v[96:97], v[98:99]
	v_pk_add_f32 v[74:75], v[80:81], v[82:83]
	v_pk_add_f32 v[76:77], v[104:105], v[106:107]
	v_pk_add_f32 v[78:79], v[84:85], v[86:87]
	v_pk_add_f32 v[58:59], v[96:97], v[104:105]
	v_pk_add_f32 v[60:61], v[98:99], v[106:107]
	v_pk_add_f32 v[72:73], v[72:73], v[74:75]
	v_pk_add_f32 v[76:77], v[76:77], v[78:79]
	v_pk_add_f32 v[54:55], v[80:81], v[84:85]
	v_pk_add_f32 v[56:57], v[82:83], v[86:87]
	v_add_f32_e32 v50, v72, v73
	v_add_f32_e32 v51, v76, v77
	v_cndmask_b32_e64 v64, v96, v80, s[20:21]
	v_cndmask_b32_e64 v65, v105, v85, s[20:21]
	s_waitcnt vmcnt(4)
	v_pk_add_f32 v[72:73], v[100:101], v[102:103]
	v_pk_add_f32 v[74:75], v[88:89], v[90:91]
	v_pk_add_f32 v[76:77], v[108:109], v[110:111]
	v_pk_add_f32 v[78:79], v[92:93], v[94:95]
	v_pk_add_f32 v[48:49], v[100:101], v[108:109]
	v_pk_add_f32 v[70:71], v[102:103], v[110:111]
	v_pk_add_f32 v[72:73], v[72:73], v[74:75]
	v_pk_add_f32 v[76:77], v[76:77], v[78:79]
	v_pk_add_f32 v[58:59], v[58:59], v[48:49]
	v_pk_add_f32 v[60:61], v[60:61], v[70:71]
	v_pk_add_f32 v[48:49], v[88:89], v[92:93]
	v_pk_add_f32 v[70:71], v[90:91], v[94:95]
	v_add_f32_e32 v52, v72, v73
	v_add_f32_e32 v53, v76, v77
	v_cndmask_b32_e64 v66, v102, v90, s[20:21]
	v_cndmask_b32_e64 v67, v111, v95, s[20:21]
	v_pk_add_f32 v[2:3], v[2:3], v[58:59]
	v_pk_add_f32 v[4:5], v[4:5], v[60:61]
	v_pk_add_f32 v[54:55], v[54:55], v[48:49]
	v_pk_add_f32 v[56:57], v[56:57], v[70:71]
	v_pk_add_f32 v[6:7], v[6:7], v[54:55]
	v_pk_add_f32 v[8:9], v[8:9], v[56:57]
	v_add_f32_dpp v50, v50, v50 quad_perm:[1,0,3,2] row_mask:0xf bank_mask:0xf
	v_add_f32_dpp v51, v51, v51 quad_perm:[1,0,3,2] row_mask:0xf bank_mask:0xf
	v_add_f32_dpp v52, v52, v52 quad_perm:[1,0,3,2] row_mask:0xf bank_mask:0xf
	v_add_f32_dpp v53, v53, v53 quad_perm:[1,0,3,2] row_mask:0xf bank_mask:0xf
	v_add_f32_dpp v50, v50, v50 quad_perm:[2,3,0,1] row_mask:0xf bank_mask:0xf
	v_add_f32_dpp v51, v51, v51 quad_perm:[2,3,0,1] row_mask:0xf bank_mask:0xf
	v_add_f32_dpp v52, v52, v52 quad_perm:[2,3,0,1] row_mask:0xf bank_mask:0xf
	v_add_f32_dpp v53, v53, v53 quad_perm:[2,3,0,1] row_mask:0xf bank_mask:0xf
	v_add_f32_dpp v50, v50, v50 row_half_mirror row_mask:0xf bank_mask:0xf
	v_add_f32_dpp v51, v51, v51 row_half_mirror row_mask:0xf bank_mask:0xf
	v_add_f32_dpp v52, v52, v52 row_half_mirror row_mask:0xf bank_mask:0xf
	v_add_f32_dpp v53, v53, v53 row_half_mirror row_mask:0xf bank_mask:0xf
	v_add_f32_dpp v50, v50, v50 row_mirror row_mask:0xf bank_mask:0xf
	v_add_f32_dpp v51, v51, v51 row_mirror row_mask:0xf bank_mask:0xf
	v_add_f32_dpp v52, v52, v52 row_mirror row_mask:0xf bank_mask:0xf
	v_add_f32_dpp v53, v53, v53 row_mirror row_mask:0xf bank_mask:0xf
	v_add_f32_dpp v50, v50, v50 row_bcast:15 row_mask:0xa bank_mask:0xf
	v_add_f32_dpp v51, v51, v51 row_bcast:15 row_mask:0xa bank_mask:0xf
	v_add_f32_dpp v52, v52, v52 row_bcast:15 row_mask:0xa bank_mask:0xf
	v_add_f32_dpp v53, v53, v53 row_bcast:15 row_mask:0xa bank_mask:0xf
	v_add_f32_dpp v50, v50, v50 row_bcast:31 row_mask:0xc bank_mask:0xf
	v_add_f32_dpp v51, v51, v51 row_bcast:31 row_mask:0xc bank_mask:0xf
	v_add_f32_dpp v52, v52, v52 row_bcast:31 row_mask:0xc bank_mask:0xf
	v_add_f32_dpp v53, v53, v53 row_bcast:31 row_mask:0xc bank_mask:0xf
	s_mov_b64 exec, s[4:5]
	global_store_dwordx4 v[44:45], v[64:67], off
	v_add_f32_e32 v72, v64, v65
	v_add_f32_e32 v73, v66, v67
	v_add_f32_e32 v72, v72, v73
	v_add_f32_e32 v42, v42, v72
	s_mov_b32 s4, 0
	s_brev_b32 s5, 1
	s_mov_b64 exec, s[4:5]
	v_lshl_add_u64 v[72:73], v[44:45], 0, s[18:19]
	global_store_dwordx4 v[72:73], v[50:53], off
	s_mov_b64 exec, -1
	s_add_u32 s15, s15, 16
	v_lshl_add_u64 v[44:45], v[44:45], 0, 64
